# GEMM-in: removed the per-phase setprio flips, one static priority raise for waves 4-7 (younger half) for the whole tile loop
# speedup vs baseline: 1.0269x; 1.0011x over previous
; __device__ __forceinline__ unsigned xb_ld(unsigned* p)              { return __hip_atomic_load(p, __ATOMIC_RELAXED, __HIP_MEMORY_SCOPE_AGENT); }
; #define G8_BAR __builtin_amdgcn_s_barrier()
; template <bool OUTP>
; __device__ __forceinline__ void gemm_phase(const Params& p, int l, char* smem, int vb, int nvb, int pm0, int M, bool fuse, int oz) {
;     ...
;     Order S; S.init(M, NP, nvb, vb);
;     const __amdgpu_buffer_rsrc_t crsrc = __builtin_amdgcn_make_buffer_rsrc((void*)Cptr, (short)0, (int)((size_t)NROW * (OUTP ? DM : LDU) * 2), 0x00020000);
;     unsigned voffA[2], voffB[2];
; #pragma unroll
;     for (int i = 0; i < 2; ++i) { int R, C; stage_rc(tid * 16 + i * 8192, R, C); const int Rb = (R & ~31) + perm32(R & 31);
;         voffA[i] = (unsigned)(R * lda + C) * 2u; voffB[i] = (unsigned)(Rb * K + C) * 2u; }
;     const size_t kstep = (size_t)(BK * 2);
;     const size_t hstepA = (size_t)HALF * lda * 2, hstepB = (size_t)HALF * K * 2;
;     const size_t tstepA = 2 * hstepA, tstepB = 2 * hstepB;
;     const unsigned ldsw = (unsigned)wid * 1024u;
;     const int aoff = lds_byte(wr * 64 + fr, fq * 8), boff = lds_byte(wc * 32 + fr, fq * 8);
;     ...
;     Unit cur, nxt; int ui = 0;
;     if (!S.next(0, cur)) return;
;     cur.pm += pm0;
;     if (OUTP) {
;         unsigned* bar = (unsigned*)(p.ws + OFF_BAR);
;         __syncthreads();
;         if (threadIdx.x == 0) {
;             XB_SPIN(xb_ld(&bar[XB_FCNT(cur.pm)]) < 256u * (unsigned)(l + 1), bar);
;             __builtin_amdgcn_fence(__ATOMIC_ACQUIRE, "agent");
;             asm volatile("s_waitcnt vmcnt(0)" ::: "memory");
;         }
;         __syncthreads();
;     }
;     f32x4 acc[2][2][4][2];
; #pragma unroll
;     for (int a = 0; a < 2; ++a)
; #pragma unroll
;         for (int b = 0; b < 2; ++b)
; #pragma unroll
;             for (int m = 0; m < 4; ++m)
; #pragma unroll
;                 for (int n = 0; n < 2; ++n) acc[a][b][m][n] = (f32x4){0.f, 0.f, 0.f, 0.f};
;     bf16x8 At[4][2], B0[2][2], B1[2][2];
;     const char* cA = (const char*)Aptr + (size_t)cur.pm * tstepA; const char* cB = (const char*)Bptr + (size_t)cur.pn * tstepB;
;     {
;         const char* a0 = cA + colb<OUTP>(0);
;         G8_STAGE(G8_SB(0, 0), cB, voffB); G8_STAGE(G8_SA(0, 0), a0, voffA); G8_STAGE(G8_SB(0, 1), cB + hstepB, voffB); G8_STAGE(G8_SA(0, 1), a0 + hstepA, voffA);
;         if (wr == 1) G8_BAR;
;         G8_WAIT_V(4); G8_BAR;
.LBB0_738:
	s_andn2_b64 vcc, exec, s[28:29]
	s_cbranch_vccnz .LBB0_782
	v_ashrrev_i32_e32 v2, 31, v9
	v_lshrrev_b32_e32 v2, 26, v2
	v_add_u32_e32 v2, v9, v2
	v_ashrrev_i32_e32 v4, 6, v2
	v_bfe_i32 v2, v9, 27, 1
	v_lshlrev_b32_e32 v1, 4, v9
	v_lshrrev_b32_e32 v2, 22, v2
	v_add_u32_e32 v2, v1, v2
	v_and_b32_e32 v2, 0xfffffc00, v2
	v_sub_u32_e32 v2, v1, v2
	v_lshrrev_b32_e32 v5, 4, v2
	v_bitop3_b32 v2, v5, v2, 32 bitop3:0x6c
	v_lshlrev_b32_e32 v5, 3, v4
	v_and_b32_e32 v6, -16, v5
	v_ashrrev_i32_e32 v5, 31, v2
	v_lshrrev_b32_e32 v5, 26, v5
	v_add_u32_e32 v7, v2, v5
	v_ashrrev_i32_e32 v5, 6, v7
	v_add_u32_e32 v8, v5, v6
	v_lshlrev_b32_e32 v6, 5, v4
	v_and_b32_e32 v10, 32, v6
	v_and_b32_e32 v6, 0xc0, v7
	v_sub_u32_e32 v2, v2, v6
	v_mov_b32_e32 v14, 1
	v_ashrrev_i16_sdwa v2, v14, sext(v2) dst_sel:DWORD dst_unused:UNUSED_PAD src0_sel:DWORD src1_sel:BYTE_0
	v_bfe_i32 v6, v2, 0, 16
	v_lshlrev_b32_e32 v2, 1, v8
	v_lshrrev_b32_e32 v7, 2, v8
	v_and_b32_e32 v11, 3, v5
	s_mov_b32 s1, 0x1fffe0
	v_and_b32_e32 v2, 24, v2
	v_and_b32_e32 v7, 4, v7
	v_and_or_b32 v11, v8, s1, v11
	v_or3_b32 v2, v11, v7, v2
	v_add_lshl_u32 v7, v10, v6, 1
	v_add_u32_e32 v1, 0x2000, v1
	v_lshl_add_u32 v132, v8, 11, v7
	v_lshl_add_u32 v2, v2, 11, v7
	v_ashrrev_i32_e32 v7, 31, v1
	v_lshrrev_b32_e32 v7, 22, v7
	v_add_u32_e32 v7, v1, v7
	v_ashrrev_i32_e32 v7, 10, v7
	v_mul_i32_i24_e32 v8, 0x400, v7
	v_sub_u32_e32 v1, v1, v8
	v_lshrrev_b32_e32 v8, 4, v1
	v_bitop3_b32 v1, v8, v1, 32 bitop3:0x6c
	v_lshlrev_b32_e32 v8, 3, v7
	v_and_b32_e32 v10, -16, v8
	v_ashrrev_i32_e32 v8, 31, v1
	v_lshrrev_b32_e32 v8, 26, v8
	v_add_u32_e32 v11, v1, v8
	v_ashrrev_i32_e32 v8, 6, v11
	v_add_u32_e32 v12, v8, v10
	v_lshlrev_b32_e32 v10, 5, v7
	v_and_b32_e32 v13, 32, v10
	v_and_b32_e32 v10, 0xc0, v11
	v_sub_u32_e32 v1, v1, v10
	v_ashrrev_i16_sdwa v1, v14, sext(v1) dst_sel:DWORD dst_unused:UNUSED_PAD src0_sel:DWORD src1_sel:BYTE_0
	v_and_b32_e32 v14, 3, v8
	s_ashr_i32 s27, s2, 6
	v_and_or_b32 v14, v12, s1, v14
	s_ashr_i32 s1, s0, 31
	s_ashr_i32 s21, s20, 31
	s_ashr_i32 s28, s2, 8
	s_lshl_b32 s3, s27, 10
	s_lshl_b64 s[24:25], s[0:1], 19
	s_lshl_b64 s[36:37], s[20:21], 19
	v_readlane_b32 s1, v254, 13
	s_add_u32 s46, s1, s36
	v_readlane_b32 s1, v254, 14
	v_bfe_i32 v10, v1, 0, 16
	v_lshlrev_b32_e32 v1, 1, v12
	v_lshrrev_b32_e32 v11, 2, v12
	s_addc_u32 s47, s1, s37
	s_add_i32 s21, s3, 0
	v_and_b32_e32 v1, 24, v1
	v_and_b32_e32 v11, 4, v11
	s_add_i32 m0, s21, 0x10000
	v_or3_b32 v1, v14, v11, v1
	v_add_lshl_u32 v11, v13, v10, 1
	global_load_lds_dwordx4 v2, s[46:47]
	s_add_i32 m0, s21, 0x12000
	v_lshl_add_u32 v136, v1, 11, v11
	s_add_u32 s38, s78, s24
	global_load_lds_dwordx4 v136, s[46:47]
	s_addc_u32 s39, s79, s25
	s_mov_b32 m0, s21
	s_add_i32 s24, s21, 0x2000
	v_lshl_add_u32 v134, v12, 11, v11
	global_load_lds_dwordx4 v132, s[38:39]
	s_mov_b32 m0, s24
	s_add_u32 s36, s46, 0x40000
	global_load_lds_dwordx4 v134, s[38:39]
	s_addc_u32 s37, s47, 0
	s_add_i32 m0, s21, 0x14000
	v_mov_b32_e32 v250, 1
	global_load_lds_dwordx4 v2, s[36:37]
	s_add_i32 m0, s21, 0x16000
	s_nop 0
	global_load_lds_dwordx4 v136, s[36:37]
	s_add_u32 s36, s38, 0x40000
	s_addc_u32 s37, s39, 0
	s_add_i32 s25, s21, 0x4000
	s_mov_b32 m0, s25
	s_add_i32 s26, s21, 0x6000
	global_load_lds_dwordx4 v132, s[36:37]
	s_mov_b32 m0, s26
	s_cmp_lg_u32 s28, 1
	global_load_lds_dwordx4 v134, s[36:37]
	s_cbranch_scc1 .LBB0_741
	s_setprio 1
	s_barrier

; #define G8_STAGE(bufoff, gbase, voff) do { _Pragma("unroll") for (int _i = 0; _i < 2; ++_i) \
;         __builtin_amdgcn_global_load_lds((const unsigned*)((const char*)(gbase) + (voff)[_i]), (G8_LAS unsigned*)(lds + (bufoff) + ldsw + _i * 8192), 16, 0, 0); } while (0)
; #define G8_LDA(dst, b, h) do { _Pragma("unroll") for (int m = 0; m < 4; ++m) _Pragma("unroll") for (int k = 0; k < 2; ++k) dst[m][k] = *(const G8_LAS bf16x8*)(lds + G8_SA(b, h) + aoff + m * 2048 + k * 1024); } while (0)
; #define G8_LDB(dst, b, h) do { _Pragma("unroll") for (int n = 0; n < 2; ++n) _Pragma("unroll") for (int k = 0; k < 2; ++k) dst[n][k] = *(const G8_LAS bf16x8*)(lds + G8_SB(b, h) + boff + n * 2048 + k * 1024); } while (0)
; #define G8_MMA(ai, bj, At, Bt) do { __builtin_amdgcn_s_setprio(1); _Pragma("unroll") for (int m = 0; m < 4; ++m) _Pragma("unroll") for (int n = 0; n < 2; ++n) _Pragma("unroll") for (int k = 0; k < 2; ++k) \
;         acc[ai][bj][m][n] = __builtin_amdgcn_mfma_f32_16x16x32_bf16(Bt[n][k], At[m][k], acc[ai][bj][m][n], 0, 0, 0); __builtin_amdgcn_s_setprio(0); } while (0)
; #define G8_WAIT_L(n) asm volatile("s_waitcnt lgkmcnt(" #n ")" ::: "memory")
; #define G8_BAR __builtin_amdgcn_s_barrier()
; #define G8_SCHED __builtin_amdgcn_sched_barrier(0)
; template <bool OUTP>
; __device__ __forceinline__ void gemm_phase(const Params& p, int l, char* smem, int vb, int nvb, int pm0, int M, bool fuse, int oz) {
;     ...
;             G8_LDB(B0, 0, 0); G8_SCHED; G8_LDA(At, 0, 0); G8_STAGE(G8_SA(1, 1), a1 + hstepA, voffA);
;             G8_WAIT_L(8); G8_BAR; G8_WAIT_L(0); G8_MMA(0, 0, At, B0); G8_BAR; G8_SCHED;
;             G8_LDB(B1, 0, 1); G8_STAGE(G8_SB(0, 0), b2, voffB);
;             G8_BAR; G8_WAIT_L(0); G8_MMA(0, 1, At, B1); G8_BAR;
;             G8_LDA(At, 0, 1); G8_STAGE(G8_SA(0, 0), a2, voffA);
;             G8_BAR; G8_WAIT_L(0); G8_MMA(1, 0, At, B0); G8_BAR; G8_SCHED;
.LBB0_746:
	s_add_u32 s46, s38, 0xfffc0080
	s_addc_u32 s47, s39, -1
	s_add_i32 s56, 0, 0x10000
	v_add_u32_e32 v146, s56, v148
	ds_read_b128 v[142:145], v146
	ds_read_b128 v[152:155], v146 offset:1024
	ds_read_b128 v[156:159], v146 offset:2048
	ds_read_b128 v[160:163], v146 offset:3072
	s_cmp_eq_u32 s55, 12
	s_cselect_b32 s49, s1, s47
	s_cselect_b32 s48, s41, s46
	s_cselect_b32 s47, s29, s54
	s_cselect_b32 s46, s52, s53
	v_lshl_add_u64 v[146:147], s[38:39], 0, v[138:139]
	s_add_i32 m0, s21, 0xc000
	ds_read_b128 v[164:167], v150
	ds_read_b128 v[168:171], v150 offset:1024
	ds_read_b128 v[172:175], v150 offset:2048
	ds_read_b128 v[176:179], v150 offset:3072
	ds_read_b128 v[180:183], v150 offset:4096
	ds_read_b128 v[184:187], v150 offset:5120
	ds_read_b128 v[188:191], v150 offset:6144
	ds_read_b128 v[192:195], v150 offset:7168
	global_load_lds_dwordx4 v[146:147], off
	v_lshl_add_u64 v[146:147], s[38:39], 0, v[140:141]
	s_add_i32 m0, s21, 0xe000
	s_nop 0
	global_load_lds_dwordx4 v[146:147], off
	s_waitcnt lgkmcnt(8)
	s_barrier
	s_waitcnt lgkmcnt(0)
	s_waitcnt lgkmcnt(0)
	v_mfma_f32_16x16x32_bf16 v[128:131], v[142:145], v[164:167], v[128:131]
	v_mfma_f32_16x16x32_bf16 v[124:127], v[156:159], v[164:167], v[124:127]
	v_mfma_f32_16x16x32_bf16 v[120:123], v[142:145], v[172:175], v[120:123]
	v_mfma_f32_16x16x32_bf16 v[112:115], v[156:159], v[172:175], v[112:115]
	v_mfma_f32_16x16x32_bf16 v[104:107], v[142:145], v[180:183], v[104:107]
	v_mfma_f32_16x16x32_bf16 v[96:99], v[156:159], v[180:183], v[96:99]
	v_mfma_f32_16x16x32_bf16 v[88:91], v[142:145], v[188:191], v[88:91]
	v_mfma_f32_16x16x32_bf16 v[80:83], v[156:159], v[188:191], v[80:83]
	v_mfma_f32_16x16x32_bf16 v[128:131], v[152:155], v[168:171], v[128:131]
	v_mfma_f32_16x16x32_bf16 v[124:127], v[160:163], v[168:171], v[124:127]
	v_mfma_f32_16x16x32_bf16 v[120:123], v[152:155], v[176:179], v[120:123]
	v_mfma_f32_16x16x32_bf16 v[112:115], v[160:163], v[176:179], v[112:115]
	v_mfma_f32_16x16x32_bf16 v[104:107], v[152:155], v[184:187], v[104:107]
	v_mfma_f32_16x16x32_bf16 v[96:99], v[160:163], v[184:187], v[96:99]
	v_mfma_f32_16x16x32_bf16 v[88:91], v[152:155], v[192:195], v[88:91]
	v_mfma_f32_16x16x32_bf16 v[80:83], v[160:163], v[192:195], v[80:83]
	s_barrier
	s_add_i32 s58, 0, 0x14000
	v_add_u32_e32 v146, s58, v148
	s_add_i32 s56, s56, s3
	ds_read_b128 v[202:205], v146
	ds_read_b128 v[206:209], v146 offset:1024
	ds_read_b128 v[210:213], v146 offset:2048
	ds_read_b128 v[214:217], v146 offset:3072
	v_lshl_add_u64 v[146:147], s[46:47], 0, v[2:3]
	s_mov_b32 m0, s56
	v_lshl_add_u64 v[218:219], s[46:47], 0, v[136:137]
	global_load_lds_dwordx4 v[146:147], off
	s_add_i32 m0, s56, 0x2000
	s_nop 0
	global_load_lds_dwordx4 v[218:219], off
	s_barrier
	s_waitcnt lgkmcnt(0)
	s_waitcnt lgkmcnt(0)
	v_mfma_f32_16x16x32_bf16 v[116:119], v[202:205], v[164:167], v[116:119]
	v_mfma_f32_16x16x32_bf16 v[108:111], v[210:213], v[164:167], v[108:111]
	v_mfma_f32_16x16x32_bf16 v[100:103], v[202:205], v[172:175], v[100:103]
	v_mfma_f32_16x16x32_bf16 v[92:95], v[210:213], v[172:175], v[92:95]
	v_mfma_f32_16x16x32_bf16 v[84:87], v[202:205], v[180:183], v[84:87]
	v_mfma_f32_16x16x32_bf16 v[76:79], v[210:213], v[180:183], v[76:79]
	v_mfma_f32_16x16x32_bf16 v[72:75], v[202:205], v[188:191], v[72:75]
	v_mfma_f32_16x16x32_bf16 v[68:71], v[210:213], v[188:191], v[68:71]
	v_mfma_f32_16x16x32_bf16 v[116:119], v[206:209], v[168:171], v[116:119]
	v_mfma_f32_16x16x32_bf16 v[108:111], v[214:217], v[168:171], v[108:111]
	v_mfma_f32_16x16x32_bf16 v[100:103], v[206:209], v[176:179], v[100:103]
	v_mfma_f32_16x16x32_bf16 v[92:95], v[214:217], v[176:179], v[92:95]
	v_mfma_f32_16x16x32_bf16 v[84:87], v[206:209], v[184:187], v[84:87]
	v_mfma_f32_16x16x32_bf16 v[76:79], v[214:217], v[184:187], v[76:79]
	v_mfma_f32_16x16x32_bf16 v[72:75], v[206:209], v[192:195], v[72:75]
	v_mfma_f32_16x16x32_bf16 v[68:71], v[214:217], v[192:195], v[68:71]
	s_mov_b32 m0, s21
	v_lshl_add_u64 v[220:221], s[48:49], 0, v[132:133]
	s_barrier
	ds_read_b128 v[164:167], v150 offset:16384
	ds_read_b128 v[168:171], v150 offset:17408
	ds_read_b128 v[172:175], v150 offset:18432
	ds_read_b128 v[176:179], v150 offset:19456
	ds_read_b128 v[180:183], v150 offset:20480
	ds_read_b128 v[184:187], v150 offset:21504
	ds_read_b128 v[188:191], v150 offset:22528
	ds_read_b128 v[192:195], v150 offset:23552
	global_load_lds_dwordx4 v[220:221], off
	v_lshl_add_u64 v[222:223], s[48:49], 0, v[134:135]
	s_mov_b32 m0, s24
	s_nop 0
	global_load_lds_dwordx4 v[222:223], off
	s_barrier
	s_waitcnt lgkmcnt(0)
	s_waitcnt lgkmcnt(0)
	v_mfma_f32_16x16x32_bf16 v[64:67], v[142:145], v[164:167], v[64:67]
	v_mfma_f32_16x16x32_bf16 v[60:63], v[156:159], v[164:167], v[60:63]
	v_mfma_f32_16x16x32_bf16 v[56:59], v[142:145], v[172:175], v[56:59]
	v_mfma_f32_16x16x32_bf16 v[48:51], v[156:159], v[172:175], v[48:51]
	v_mfma_f32_16x16x32_bf16 v[40:43], v[142:145], v[180:183], v[40:43]
	v_mfma_f32_16x16x32_bf16 v[32:35], v[156:159], v[180:183], v[32:35]
	v_mfma_f32_16x16x32_bf16 v[24:27], v[142:145], v[188:191], v[24:27]
	v_mfma_f32_16x16x32_bf16 v[16:19], v[156:159], v[188:191], v[16:19]
	v_mfma_f32_16x16x32_bf16 v[64:67], v[152:155], v[168:171], v[64:67]
	v_mfma_f32_16x16x32_bf16 v[60:63], v[160:163], v[168:171], v[60:63]
	v_mfma_f32_16x16x32_bf16 v[56:59], v[152:155], v[176:179], v[56:59]
	v_mfma_f32_16x16x32_bf16 v[48:51], v[160:163], v[176:179], v[48:51]
	v_mfma_f32_16x16x32_bf16 v[40:43], v[152:155], v[184:187], v[40:43]
	v_mfma_f32_16x16x32_bf16 v[32:35], v[160:163], v[184:187], v[32:35]
	v_mfma_f32_16x16x32_bf16 v[24:27], v[152:155], v[192:195], v[24:27]
	v_mfma_f32_16x16x32_bf16 v[16:19], v[160:163], v[192:195], v[16:19]
	s_barrier
; #define G8_STAGE(bufoff, gbase, voff) do { _Pragma("unroll") for (int _i = 0; _i < 2; ++_i) \
;         __builtin_amdgcn_global_load_lds((const unsigned*)((const char*)(gbase) + (voff)[_i]), (G8_LAS unsigned*)(lds + (bufoff) + ldsw + _i * 8192), 16, 0, 0); } while (0)
; #define G8_LDA(dst, b, h) do { _Pragma("unroll") for (int m = 0; m < 4; ++m) _Pragma("unroll") for (int k = 0; k < 2; ++k) dst[m][k] = *(const G8_LAS bf16x8*)(lds + G8_SA(b, h) + aoff + m * 2048 + k * 1024); } while (0)
; #define G8_LDB(dst, b, h) do { _Pragma("unroll") for (int n = 0; n < 2; ++n) _Pragma("unroll") for (int k = 0; k < 2; ++k) dst[n][k] = *(const G8_LAS bf16x8*)(lds + G8_SB(b, h) + boff + n * 2048 + k * 1024); } while (0)
; #define G8_MMA(ai, bj, At, Bt) do { __builtin_amdgcn_s_setprio(1); _Pragma("unroll") for (int m = 0; m < 4; ++m) _Pragma("unroll") for (int n = 0; n < 2; ++n) _Pragma("unroll") for (int k = 0; k < 2; ++k) \
;         acc[ai][bj][m][n] = __builtin_amdgcn_mfma_f32_16x16x32_bf16(Bt[n][k], At[m][k], acc[ai][bj][m][n], 0, 0, 0); __builtin_amdgcn_s_setprio(0); } while (0)
; #define G8_WAIT_V(n) asm volatile("s_waitcnt vmcnt(" #n ")" ::: "memory")
; #define G8_WAIT_L(n) asm volatile("s_waitcnt lgkmcnt(" #n ")" ::: "memory")
; #define G8_BAR __builtin_amdgcn_s_barrier()
; #define G8_SCHED __builtin_amdgcn_sched_barrier(0)
; template <bool OUTP>
; __device__ __forceinline__ void gemm_phase(const Params& p, int l, char* smem, int vb, int nvb, int pm0, int M, bool fuse, int oz) {
;     ...
;             G8_STAGE(G8_SB(0, 1), b2 + hstepB, voffB);
;             G8_WAIT_V(6); G8_BAR; G8_MMA(1, 1, At, B1); G8_BAR;
;             G8_LDB(B0, 1, 0); G8_SCHED; G8_LDA(At, 1, 0); G8_STAGE(G8_SA(0, 1), a2 + hstepA, voffA);
;             G8_WAIT_L(8); G8_BAR; G8_WAIT_L(0); G8_MMA(0, 0, At, B0); G8_BAR; G8_SCHED;
;             G8_LDB(B1, 1, 1); G8_STAGE(G8_SB(1, 0), b3, voffB);
;             G8_BAR; G8_WAIT_L(0); G8_MMA(0, 1, At, B1); G8_BAR;
	s_add_u32 s56, s46, 0x40000
	s_addc_u32 s57, s47, 0
	s_add_i32 s58, s58, s3
	v_lshl_add_u64 v[142:143], s[56:57], 0, v[2:3]
	s_mov_b32 m0, s58
	s_nop 0
	global_load_lds_dwordx4 v[142:143], off
	v_lshl_add_u64 v[142:143], s[56:57], 0, v[136:137]
	s_add_i32 m0, s58, 0x2000
	s_nop 0
	global_load_lds_dwordx4 v[142:143], off
	s_waitcnt vmcnt(6)
	s_barrier
	v_mfma_f32_16x16x32_bf16 v[52:55], v[202:205], v[164:167], v[52:55]
	v_mfma_f32_16x16x32_bf16 v[44:47], v[210:213], v[164:167], v[44:47]
	v_mfma_f32_16x16x32_bf16 v[36:39], v[202:205], v[172:175], v[36:39]
	v_mfma_f32_16x16x32_bf16 v[28:31], v[210:213], v[172:175], v[28:31]
	v_mfma_f32_16x16x32_bf16 v[20:23], v[202:205], v[180:183], v[20:23]
	v_mfma_f32_16x16x32_bf16 v[12:15], v[210:213], v[180:183], v[12:15]
	v_mfma_f32_16x16x32_bf16 v[8:11], v[202:205], v[188:191], v[8:11]
	v_mfma_f32_16x16x32_bf16 v[4:7], v[210:213], v[188:191], v[4:7]
	v_mfma_f32_16x16x32_bf16 v[52:55], v[206:209], v[168:171], v[52:55]
	v_mfma_f32_16x16x32_bf16 v[44:47], v[214:217], v[168:171], v[44:47]
	v_mfma_f32_16x16x32_bf16 v[36:39], v[206:209], v[176:179], v[36:39]
	v_mfma_f32_16x16x32_bf16 v[28:31], v[214:217], v[176:179], v[28:31]
	v_mfma_f32_16x16x32_bf16 v[20:23], v[206:209], v[184:187], v[20:23]
	v_mfma_f32_16x16x32_bf16 v[12:15], v[214:217], v[184:187], v[12:15]
	v_mfma_f32_16x16x32_bf16 v[8:11], v[206:209], v[192:195], v[8:11]
	v_mfma_f32_16x16x32_bf16 v[4:7], v[214:217], v[192:195], v[4:7]
	s_add_i32 s56, 0, 0x18000
	v_add_u32_e32 v151, s56, v148
	s_barrier
	ds_read_b128 v[142:145], v151
	ds_read_b128 v[152:155], v151 offset:1024
	ds_read_b128 v[156:159], v151 offset:2048
	ds_read_b128 v[160:163], v151 offset:3072
	s_add_u32 s48, s48, 0x40000
	s_addc_u32 s49, s49, 0
	s_mov_b32 m0, s25
	v_lshl_add_u64 v[202:203], s[48:49], 0, v[132:133]
	ds_read_b128 v[164:167], v150 offset:32768
	ds_read_b128 v[168:171], v150 offset:33792
	ds_read_b128 v[172:175], v150 offset:34816
	ds_read_b128 v[176:179], v150 offset:35840
	ds_read_b128 v[180:183], v150 offset:36864
	ds_read_b128 v[184:187], v150 offset:37888
	ds_read_b128 v[188:191], v150 offset:38912
	ds_read_b128 v[192:195], v150 offset:39936
	global_load_lds_dwordx4 v[202:203], off
	v_lshl_add_u64 v[202:203], s[48:49], 0, v[134:135]
	s_mov_b32 m0, s26
	s_nop 0
	global_load_lds_dwordx4 v[202:203], off
	s_waitcnt lgkmcnt(8)
	s_barrier
	s_waitcnt lgkmcnt(0)
	s_waitcnt lgkmcnt(0)
	v_mfma_f32_16x16x32_bf16 v[128:131], v[142:145], v[164:167], v[128:131]
	v_mfma_f32_16x16x32_bf16 v[124:127], v[156:159], v[164:167], v[124:127]
	v_mfma_f32_16x16x32_bf16 v[120:123], v[142:145], v[172:175], v[120:123]
	v_mfma_f32_16x16x32_bf16 v[112:115], v[156:159], v[172:175], v[112:115]
	v_mfma_f32_16x16x32_bf16 v[104:107], v[142:145], v[180:183], v[104:107]
	v_mfma_f32_16x16x32_bf16 v[96:99], v[156:159], v[180:183], v[96:99]
	v_mfma_f32_16x16x32_bf16 v[88:91], v[142:145], v[188:191], v[88:91]
	v_mfma_f32_16x16x32_bf16 v[80:83], v[156:159], v[188:191], v[80:83]
	v_mfma_f32_16x16x32_bf16 v[128:131], v[152:155], v[168:171], v[128:131]
	v_mfma_f32_16x16x32_bf16 v[124:127], v[160:163], v[168:171], v[124:127]
	v_mfma_f32_16x16x32_bf16 v[120:123], v[152:155], v[176:179], v[120:123]
	v_mfma_f32_16x16x32_bf16 v[112:115], v[160:163], v[176:179], v[112:115]
	v_mfma_f32_16x16x32_bf16 v[104:107], v[152:155], v[184:187], v[104:107]
	v_mfma_f32_16x16x32_bf16 v[96:99], v[160:163], v[184:187], v[96:99]
	v_mfma_f32_16x16x32_bf16 v[88:91], v[152:155], v[192:195], v[88:91]
	v_mfma_f32_16x16x32_bf16 v[80:83], v[160:163], v[192:195], v[80:83]
	s_barrier
	s_add_i32 s48, 0, 0x1c000
	s_add_i32 s49, s56, s3
	v_add_u32_e32 v151, s48, v148
	v_lshl_add_u64 v[146:147], v[146:147], 0, s[90:91]
	s_mov_b32 m0, s49
	ds_read_b128 v[202:205], v151
	ds_read_b128 v[206:209], v151 offset:1024
	ds_read_b128 v[210:213], v151 offset:2048
	ds_read_b128 v[214:217], v151 offset:3072
	global_load_lds_dwordx4 v[146:147], off
	v_lshl_add_u64 v[146:147], v[218:219], 0, s[90:91]
	s_add_i32 m0, s49, 0x2000
	s_nop 0
	global_load_lds_dwordx4 v[146:147], off
	s_barrier
; #define G8_STAGE(bufoff, gbase, voff) do { _Pragma("unroll") for (int _i = 0; _i < 2; ++_i) \
;         __builtin_amdgcn_global_load_lds((const unsigned*)((const char*)(gbase) + (voff)[_i]), (G8_LAS unsigned*)(lds + (bufoff) + ldsw + _i * 8192), 16, 0, 0); } while (0)
; #define G8_LDA(dst, b, h) do { _Pragma("unroll") for (int m = 0; m < 4; ++m) _Pragma("unroll") for (int k = 0; k < 2; ++k) dst[m][k] = *(const G8_LAS bf16x8*)(lds + G8_SA(b, h) + aoff + m * 2048 + k * 1024); } while (0)
; #define G8_MMA(ai, bj, At, Bt) do { __builtin_amdgcn_s_setprio(1); _Pragma("unroll") for (int m = 0; m < 4; ++m) _Pragma("unroll") for (int n = 0; n < 2; ++n) _Pragma("unroll") for (int k = 0; k < 2; ++k) \
;         acc[ai][bj][m][n] = __builtin_amdgcn_mfma_f32_16x16x32_bf16(Bt[n][k], At[m][k], acc[ai][bj][m][n], 0, 0, 0); __builtin_amdgcn_s_setprio(0); } while (0)
; #define G8_BAR __builtin_amdgcn_s_barrier()
; template <bool OUTP>
; __device__ __forceinline__ void gemm_phase(const Params& p, int l, char* smem, int vb, int nvb, int pm0, int M, bool fuse, int oz) {
;     ...
;             G8_BAR; G8_WAIT_L(0); G8_MMA(0, 1, At, B1); G8_BAR;
;             G8_LDA(At, 1, 1); G8_STAGE(G8_SA(1, 0), a3, voffA);
;             G8_BAR; G8_WAIT_L(0); G8_MMA(1, 0, At, B0); G8_BAR; G8_SCHED;
;             G8_STAGE(G8_SB(1, 1), b3 + hstepB, voffB);
;             G8_WAIT_V(6); G8_BAR; G8_MMA(1, 1, At, B1); G8_BAR;
;         }
;         if (!(OUTP && fuse)) {
;             const int row0 = cur.pm * BM + wr * 64 + fr, col0 = cur.pn * BM + wc * 32 + 8 * fq;
; #pragma unroll
;             for (int ai = 0; ai < 2; ++ai)
; #pragma unroll
;                 for (int m = 0; m < 4; ++m) {
;                     bf16_t* rowp = Cptr + (size_t)(row0 + ai * HALF + m * 16) * ldc + col0;
; #pragma unroll
;                     for (int bj = 0; bj < 2; ++bj) {
;                         if (col0 + bj * HALF < N) {
;                             const f32x4 v0 = acc[ai][bj][m][0], v1 = acc[ai][bj][m][1];
;                             u32x4 w = {cvt_pk(v0[0], v0[1]), cvt_pk(v0[2], v0[3]), cvt_pk(v1[0], v1[1]), cvt_pk(v1[2], v1[3])};
;                             if (OUTP) {
;                                 __builtin_amdgcn_raw_buffer_store_b128(w, crsrc, (int)(((size_t)(row0 + ai * HALF + m * 16) * ldc + col0 + bj * HALF) * 2), 0, 16);
;                             } else *(u32x4*)(rowp + bj * HALF) = w;
	s_waitcnt lgkmcnt(0)
	s_waitcnt lgkmcnt(0)
	v_mfma_f32_16x16x32_bf16 v[116:119], v[202:205], v[164:167], v[116:119]
	v_mfma_f32_16x16x32_bf16 v[108:111], v[210:213], v[164:167], v[108:111]
	v_mfma_f32_16x16x32_bf16 v[100:103], v[202:205], v[172:175], v[100:103]
	v_mfma_f32_16x16x32_bf16 v[92:95], v[210:213], v[172:175], v[92:95]
	v_mfma_f32_16x16x32_bf16 v[84:87], v[202:205], v[180:183], v[84:87]
	v_mfma_f32_16x16x32_bf16 v[76:79], v[210:213], v[180:183], v[76:79]
	v_mfma_f32_16x16x32_bf16 v[72:75], v[202:205], v[188:191], v[72:75]
	v_mfma_f32_16x16x32_bf16 v[68:71], v[210:213], v[188:191], v[68:71]
	v_mfma_f32_16x16x32_bf16 v[116:119], v[206:209], v[168:171], v[116:119]
	v_mfma_f32_16x16x32_bf16 v[108:111], v[214:217], v[168:171], v[108:111]
	v_mfma_f32_16x16x32_bf16 v[100:103], v[206:209], v[176:179], v[100:103]
	v_mfma_f32_16x16x32_bf16 v[92:95], v[214:217], v[176:179], v[92:95]
	v_mfma_f32_16x16x32_bf16 v[84:87], v[206:209], v[184:187], v[84:87]
	v_mfma_f32_16x16x32_bf16 v[76:79], v[214:217], v[184:187], v[76:79]
	v_mfma_f32_16x16x32_bf16 v[72:75], v[206:209], v[192:195], v[72:75]
	v_mfma_f32_16x16x32_bf16 v[68:71], v[214:217], v[192:195], v[68:71]
	s_mov_b32 m0, s31
	v_lshl_add_u64 v[146:147], v[220:221], 0, s[90:91]
	s_barrier
	ds_read_b128 v[164:167], v150 offset:49152
	ds_read_b128 v[168:171], v150 offset:50176
	ds_read_b128 v[172:175], v150 offset:51200
	ds_read_b128 v[176:179], v150 offset:52224
	ds_read_b128 v[180:183], v150 offset:53248
	ds_read_b128 v[184:187], v150 offset:54272
	ds_read_b128 v[188:191], v150 offset:55296
	ds_read_b128 v[192:195], v150 offset:56320
	global_load_lds_dwordx4 v[146:147], off
	v_lshl_add_u64 v[146:147], v[222:223], 0, s[90:91]
	s_mov_b32 m0, s50
	s_nop 0
	global_load_lds_dwordx4 v[146:147], off
	s_barrier
	s_waitcnt lgkmcnt(0)
	s_waitcnt lgkmcnt(0)
	v_mfma_f32_16x16x32_bf16 v[64:67], v[142:145], v[164:167], v[64:67]
	v_mfma_f32_16x16x32_bf16 v[60:63], v[156:159], v[164:167], v[60:63]
	v_mfma_f32_16x16x32_bf16 v[56:59], v[142:145], v[172:175], v[56:59]
	v_mfma_f32_16x16x32_bf16 v[48:51], v[156:159], v[172:175], v[48:51]
	v_mfma_f32_16x16x32_bf16 v[40:43], v[142:145], v[180:183], v[40:43]
	v_mfma_f32_16x16x32_bf16 v[32:35], v[156:159], v[180:183], v[32:35]
	v_mfma_f32_16x16x32_bf16 v[24:27], v[142:145], v[188:191], v[24:27]
	v_mfma_f32_16x16x32_bf16 v[16:19], v[156:159], v[188:191], v[16:19]
	v_mfma_f32_16x16x32_bf16 v[64:67], v[152:155], v[168:171], v[64:67]
	v_mfma_f32_16x16x32_bf16 v[60:63], v[160:163], v[168:171], v[60:63]
	v_mfma_f32_16x16x32_bf16 v[56:59], v[152:155], v[176:179], v[56:59]
	v_mfma_f32_16x16x32_bf16 v[48:51], v[160:163], v[176:179], v[48:51]
	v_mfma_f32_16x16x32_bf16 v[40:43], v[152:155], v[184:187], v[40:43]
	v_mfma_f32_16x16x32_bf16 v[32:35], v[160:163], v[184:187], v[32:35]
	v_mfma_f32_16x16x32_bf16 v[24:27], v[152:155], v[192:195], v[24:27]
	v_mfma_f32_16x16x32_bf16 v[16:19], v[160:163], v[192:195], v[16:19]
	s_barrier
	s_add_u32 s46, s46, 0x40080
	s_addc_u32 s47, s47, 0
	s_add_i32 s48, s48, s3
	v_lshl_add_u64 v[142:143], s[46:47], 0, v[2:3]
	s_mov_b32 m0, s48
	s_nop 0
	global_load_lds_dwordx4 v[142:143], off
	v_lshl_add_u64 v[142:143], s[46:47], 0, v[136:137]
	s_add_i32 m0, s48, 0x2000
	s_nop 0
	global_load_lds_dwordx4 v[142:143], off
	s_waitcnt vmcnt(6)
	s_barrier
	v_mfma_f32_16x16x32_bf16 v[52:55], v[202:205], v[164:167], v[52:55]
	v_mfma_f32_16x16x32_bf16 v[44:47], v[210:213], v[164:167], v[44:47]
	v_mfma_f32_16x16x32_bf16 v[36:39], v[202:205], v[172:175], v[36:39]
	v_mfma_f32_16x16x32_bf16 v[28:31], v[210:213], v[172:175], v[28:31]
	v_mfma_f32_16x16x32_bf16 v[20:23], v[202:205], v[180:183], v[20:23]
	v_mfma_f32_16x16x32_bf16 v[12:15], v[210:213], v[180:183], v[12:15]
	v_mfma_f32_16x16x32_bf16 v[8:11], v[202:205], v[188:191], v[8:11]
	v_mfma_f32_16x16x32_bf16 v[4:7], v[210:213], v[188:191], v[4:7]
	v_mfma_f32_16x16x32_bf16 v[52:55], v[206:209], v[168:171], v[52:55]
	v_mfma_f32_16x16x32_bf16 v[44:47], v[214:217], v[168:171], v[44:47]
	v_mfma_f32_16x16x32_bf16 v[36:39], v[206:209], v[176:179], v[36:39]
	v_mfma_f32_16x16x32_bf16 v[28:31], v[214:217], v[176:179], v[28:31]
	v_mfma_f32_16x16x32_bf16 v[20:23], v[206:209], v[184:187], v[20:23]
	v_mfma_f32_16x16x32_bf16 v[12:15], v[214:217], v[184:187], v[12:15]
	v_mfma_f32_16x16x32_bf16 v[8:11], v[206:209], v[192:195], v[8:11]
	v_mfma_f32_16x16x32_bf16 v[4:7], v[214:217], v[192:195], v[4:7]
	s_add_i32 s55, s55, 2
	s_add_u32 s38, s38, 0x100
	s_addc_u32 s39, s39, 0
	s_add_u32 s53, s53, 0x100
	s_addc_u32 s54, s54, 0
	s_cmp_gt_u32 s55, 13
	s_barrier
	s_cbranch_scc0 .LBB0_746
	v_lshl_or_b32 v146, s20, 8, v149
	v_ashrrev_i32_e32 v147, 31, v146
	v_lshl_add_u32 v151, s0, 8, v1
	v_lshl_add_u64 v[142:143], v[146:147], 1, s[34:35]
	v_mad_i64_i32 v[144:145], s[0:1], v151, s92, v[142:143]
	s_movk_i32 s0, 0xd10
	s_nop 0
	v_cmp_gt_i32_e32 vcc, s0, v146
	s_and_saveexec_b64 s[0:1], vcc
	s_cbranch_execz .LBB0_749
	v_cvt_pk_bf16_f32 v128, v128, v129
	v_cvt_pk_bf16_f32 v129, v130, v131
	v_cvt_pk_bf16_f32 v130, v124, v125
	v_cvt_pk_bf16_f32 v131, v126, v127
	global_store_dwordx4 v[144:145], v[128:131], off

; #define G8_WAIT_V(n) asm volatile("s_waitcnt vmcnt(" #n ")" ::: "memory")
; #define G8_BAR __builtin_amdgcn_s_barrier()
; template <bool OUTP>
; __device__ __forceinline__ void gemm_phase(const Params& p, int l, char* smem, int vb, int nvb, int pm0, int M, bool fuse, int oz) {
;     ...
;     G8_WAIT_V(0);
;     if (wr == 0) G8_BAR;
;     G8_BAR;
.LBB0_781:
	s_setprio 0
	s_barrier
